# baseline (speedup 1.0000x reference)
.Lj_got:
	v_cvt_pk_bf16_f32 v214, v204, v204
	v_lshlrev_b32_e32 v215, 16, v214
	v_sub_f32_e32 v215, v204, v215
	v_add_u32_e32 v238, s38, v225
	v_cvt_pk_bf16_f32 v215, v215, v215
	ds_write_b16 v238, v214
	ds_write_b16 v238, v215 offset:2176
	v_cvt_pk_bf16_f32 v210, v202, v202
	v_lshlrev_b32_e32 v211, 16, v210
	v_sub_f32_e32 v211, v202, v211
	v_add_u32_e32 v238, s38, v226
	v_cvt_pk_bf16_f32 v211, v211, v211
	ds_write_b16 v238, v210
	ds_write_b16 v238, v211 offset:2176
	v_cvt_pk_bf16_f32 v212, v218, v218
	v_lshlrev_b32_e32 v213, 16, v212
	v_sub_f32_e32 v213, v218, v213
	v_add_u32_e32 v238, s38, v227
	v_cvt_pk_bf16_f32 v213, v213, v213
	ds_write_b16 v238, v212
	ds_write_b16 v238, v213 offset:2176
.Lj_gdone:
	s_waitcnt lgkmcnt(0)
	s_barrier
	v_add_u32_e32 v240, s45, v229
	v_add_u32_e32 v241, s44, v229
	v_add_u32_e32 v242, s60, v229
	ds_read_b128 v[150:153], v240 offset:0
	ds_read_b128 v[194:197], v240 offset:128
	ds_read_b128 v[198:201], v240 offset:256
	ds_read_b128 v[232:235], v240 offset:384
	s_cmp_eq_u32 s20, 0
	s_cselect_b64 s[36:37], -1, 0
	s_add_i32 s29, s20, 1
	s_and_b32 s14, s29, 1
	s_lshl_b32 s10, s14, 13
	s_mov_b32 s11, 0
	v_lshl_add_u64 v[250:251], v[0:1], 0, s[10:11]
	s_mul_i32 s15, s14, 0x1100
	v_add_u32_e32 v243, s15, v228
	v_mov_b32_e32 v253, s29
	s_waitcnt lgkmcnt(3)
	v_smfmac_f32_16x16x64_bf16 v[162:165], v[150:153], v[174:181], v223
	ds_read_b128 v[174:177], v224 offset:14336
	v_smfmac_f32_16x16x64_bf16 v[146:149], v[150:153], v[98:105], v223
	ds_read_b128 v[178:181], v224 offset:15360
	v_smfmac_f32_16x16x64_bf16 v[154:157], v[150:153], v[114:121], v223
	v_smfmac_f32_16x16x64_bf16 v[158:161], v[150:153], v[130:137], v223
	ds_read_b128 v[150:153], v241 offset:0
	s_waitcnt lgkmcnt(5)
	v_smfmac_f32_16x16x64_bf16 v[162:165], v[194:197], v[182:189], v223
	ds_read_b128 v[182:185], v224 offset:16384
	v_smfmac_f32_16x16x64_bf16 v[146:149], v[194:197], v[106:113], v223
	ds_read_b128 v[186:189], v224 offset:17408
	v_smfmac_f32_16x16x64_bf16 v[154:157], v[194:197], v[122:129], v223
	v_smfmac_f32_16x16x64_bf16 v[158:161], v[194:197], v[138:145], v223
	ds_read_b128 v[194:197], v241 offset:128
	s_waitcnt lgkmcnt(7)
	v_smfmac_f32_16x16x64_bf16 v[162:165], v[198:201], v[166:173], v223
	ds_read_b128 v[166:169], v224 offset:18432
	v_smfmac_f32_16x16x64_bf16 v[146:149], v[198:201], a[0:7], v223
	ds_read_b128 v[170:173], v224 offset:19456
	v_smfmac_f32_16x16x64_bf16 v[154:157], v[198:201], a[16:23], v223
	v_smfmac_f32_16x16x64_bf16 v[158:161], v[198:201], a[32:39], v223
	ds_read_b128 v[198:201], v241 offset:256
	s_waitcnt lgkmcnt(7)
	v_smfmac_f32_16x16x64_bf16 v[162:165], v[232:235], v[174:181], v223
	ds_read_b128 v[174:177], v224 offset:20480
	v_smfmac_f32_16x16x64_bf16 v[146:149], v[232:235], a[8:15], v223
	ds_read_b128 v[178:181], v224 offset:21504
	v_smfmac_f32_16x16x64_bf16 v[154:157], v[232:235], a[24:31], v223
	v_smfmac_f32_16x16x64_bf16 v[158:161], v[232:235], a[40:47], v223
	ds_read_b128 v[232:235], v241 offset:384
	s_waitcnt lgkmcnt(7)
	v_smfmac_f32_16x16x64_bf16 v[162:165], v[150:153], v[182:189], v223
	ds_read_b128 v[182:185], v224 offset:22528
	v_smfmac_f32_16x16x64_bf16 v[146:149], v[150:153], a[48:55], v223
	ds_read_b128 v[186:189], v224 offset:23552
	v_smfmac_f32_16x16x64_bf16 v[154:157], v[150:153], a[64:71], v223
	v_smfmac_f32_16x16x64_bf16 v[158:161], v[150:153], a[80:87], v223
	ds_read_b128 v[150:153], v242 offset:0
	s_waitcnt lgkmcnt(7)
	v_smfmac_f32_16x16x64_bf16 v[162:165], v[194:197], v[166:173], v223
	ds_read_b128 v[166:169], v224 offset:24576
	v_smfmac_f32_16x16x64_bf16 v[146:149], v[194:197], a[56:63], v223
	ds_read_b128 v[170:173], v224 offset:25600
	v_smfmac_f32_16x16x64_bf16 v[154:157], v[194:197], a[72:79], v223
	v_smfmac_f32_16x16x64_bf16 v[158:161], v[194:197], a[88:95], v223
	ds_read_b128 v[194:197], v242 offset:128
	s_waitcnt lgkmcnt(7)
	v_smfmac_f32_16x16x64_bf16 v[162:165], v[198:201], v[174:181], v223
	ds_read_b128 v[174:177], v224 offset:26624
	v_smfmac_f32_16x16x64_bf16 v[146:149], v[198:201], a[96:103], v223
	ds_read_b128 v[178:181], v224 offset:27648
	v_smfmac_f32_16x16x64_bf16 v[154:157], v[198:201], a[112:119], v223
	v_smfmac_f32_16x16x64_bf16 v[158:161], v[198:201], a[128:135], v223
	ds_read_b128 v[198:201], v242 offset:256
	s_waitcnt lgkmcnt(7)
	v_smfmac_f32_16x16x64_bf16 v[162:165], v[232:235], v[182:189], v223
	ds_read_b128 v[182:185], v224 offset:28672
	v_smfmac_f32_16x16x64_bf16 v[146:149], v[232:235], a[104:111], v223
	ds_read_b128 v[186:189], v224 offset:29696
	v_smfmac_f32_16x16x64_bf16 v[154:157], v[232:235], a[120:127], v223
	v_smfmac_f32_16x16x64_bf16 v[158:161], v[232:235], a[136:143], v223
	ds_read_b128 v[232:235], v242 offset:384
	s_waitcnt lgkmcnt(7)
	v_smfmac_f32_16x16x64_bf16 v[162:165], v[150:153], v[166:173], v223
	ds_read_b128 v[166:169], v224 offset:30720
	v_smfmac_f32_16x16x64_bf16 v[146:149], v[150:153], a[144:151], v223
	ds_read_b128 v[170:173], v224 offset:31744
	v_smfmac_f32_16x16x64_bf16 v[154:157], v[150:153], a[160:167], v223
	v_smfmac_f32_16x16x64_bf16 v[158:161], v[150:153], a[176:183], v223
	s_waitcnt lgkmcnt(6)
	v_smfmac_f32_16x16x64_bf16 v[162:165], v[194:197], v[174:181], v223
	ds_read_b128 v[174:177], v224 offset:2048
	v_smfmac_f32_16x16x64_bf16 v[146:149], v[194:197], a[152:159], v223
	ds_read_b128 v[178:181], v224 offset:3072
	v_smfmac_f32_16x16x64_bf16 v[154:157], v[194:197], a[168:175], v223
	v_smfmac_f32_16x16x64_bf16 v[158:161], v[194:197], a[184:191], v223
	s_waitcnt lgkmcnt(5)
	v_smfmac_f32_16x16x64_bf16 v[162:165], v[198:201], v[182:189], v223
	ds_read_b128 v[182:185], v224 offset:4096
	v_smfmac_f32_16x16x64_bf16 v[146:149], v[198:201], a[192:199], v223
	ds_read_b128 v[186:189], v224 offset:5120
	v_smfmac_f32_16x16x64_bf16 v[154:157], v[198:201], a[208:215], v223
	v_smfmac_f32_16x16x64_bf16 v[158:161], v[198:201], a[224:231], v223
	s_waitcnt lgkmcnt(4)
	v_smfmac_f32_16x16x64_bf16 v[162:165], v[232:235], v[166:173], v223
	ds_read_b128 v[166:169], v224 offset:0
	v_smfmac_f32_16x16x64_bf16 v[146:149], v[232:235], a[200:207], v223
	ds_read_b128 v[170:173], v224 offset:1024
	v_smfmac_f32_16x16x64_bf16 v[154:157], v[232:235], a[216:223], v223
	v_smfmac_f32_16x16x64_bf16 v[158:161], v[232:235], a[232:239], v223
	s_nop 5
	v_pk_add_f32 v[244:245], v[162:163], v[164:165]
	v_pk_add_f32 v[236:237], v[146:147], v[148:149]
	v_pk_add_f32 v[238:239], v[154:155], v[156:157]
	v_pk_add_f32 v[240:241], v[158:159], v[160:161]
	v_add_f32_e32 v236, v236, v237
	v_add_f32_e32 v237, v238, v239
	v_add_f32_e32 v238, v240, v241
	v_add_f32_e32 v239, v244, v245
	v_cndmask_b32_e64 v236, v236, v237, s[4:5]
	v_cndmask_b32_e64 v236, v236, v238, s[6:7]
	v_cndmask_b32_e64 v156, v236, v239, s[74:75]
	v_add_f32_e32 v236, v208, v156
	v_cndmask_b32_e64 v252, v156, v236, s[36:37]
	global_store_dwordx2 v[250:251], v[252:253], off sc1
	v_cvt_pk_bf16_f32 v237, v252, v252
	v_lshlrev_b32_e32 v238, 16, v237
	v_sub_f32_e32 v238, v252, v238
	v_cvt_pk_bf16_f32 v238, v238, v238
	ds_write_b16 v243, v237
	ds_write_b16 v243, v238 offset:2176
	v_or3_b32 v231, v214, v215, v216
	v_or3_b32 v231, v210, v211, v231
	v_or3_b32 v231, v212, v213, v231
	s_lshl_b32 s83, s70, 4
	v_and_b32_e32 v231, 0x7fff7fff, v231
	v_add_u32_e32 v239, s83, v254
	v_cmp_eq_u32_e32 vcc, 0, v231
	s_cmp_eq_u64 vcc, exec
	s_cselect_b32 s82, 1, 0
	v_mov_b32_e32 v236, s82
	ds_write_b32 v239, v236
	v_or_b32_e32 v216, v237, v238
	s_cmp_eq_u32 s20, 0
	s_cbranch_scc1 .Lj_nores
	v_mul_f32_e32 v146, v207, v156
	v_mul_f32_e32 v147, v146, v146
	s_nop 1
	v_mov_b32_dpp v147, v147 row_shr:1 row_mask:0xf bank_mask:0xf bound_ctrl:1
	v_fmac_f32_e32 v147, v146, v146
	s_nop 1
	v_add_f32_dpp v146, v147, v147 row_shr:2 row_mask:0xf bank_mask:0xf bound_ctrl:1
	v_mov_b32_e32 v147, v191
	s_nop 0
	v_add_f32_dpp v146, v146, v146 row_shr:4 row_mask:0xf bank_mask:0xf bound_ctrl:1
	s_nop 1
	v_add_f32_dpp v146, v146, v146 row_shr:8 row_mask:0xf bank_mask:0xf bound_ctrl:1
	s_nop 1
	v_mov_b32_dpp v147, v146 row_bcast:15 row_mask:0xa bank_mask:0xf
	v_add_f32_e32 v146, v146, v147
	v_mov_b32_e32 v147, v191
	s_nop 1
	v_mov_b32_dpp v147, v146 row_bcast:31 row_mask:0xc bank_mask:0xf
	s_and_saveexec_b64 s[10:11], s[8:9]
	s_lshl_b32 s14, s14, 4
	s_add_i32 s14, s42, s14
	v_add_f32_e32 v146, v146, v147
	v_mov_b32_e32 v147, s14
	ds_write_b32 v147, v146
	s_or_b64 exec, exec, s[10:11]
